# v53: v51 + KV and in-proj(1) epilogue first loads before the realign barrier; MoE-down per-tile expert lookup from the LDS table instead of a waited global load
# baseline (speedup 1.0000x reference)
.LBB0_689:
	s_add_u32 s26, s21, s10
	s_addc_u32 s27, s22, s11
	s_add_u32 s12, s26, 0x15000100
	s_addc_u32 s13, s27, 0
	s_add_u32 s14, s23, s10
	s_addc_u32 s15, s24, s11
	s_add_i32 s28, 0, 0x10000
	s_cmpk_eq_i32 s10, 0x300
	s_cselect_b32 s13, s9, s13
	s_cselect_b32 s12, s8, s12
	v_add_u32_e32 v0, s28, v38
	s_cselect_b32 s15, s7, s15
	s_cselect_b32 s14, s6, s14
	s_add_i32 s29, 0, 0x14000
	ds_read_b128 v[138:141], v0
	ds_read_b128 v[142:145], v0 offset:1024
	ds_read_b128 v[146:149], v0 offset:2048
	ds_read_b128 v[150:153], v0 offset:3072
	v_add_u32_e32 v0, s29, v38
	ds_read_b128 v[154:157], v0
	ds_read_b128 v[158:161], v0 offset:1024
	ds_read_b128 v[162:165], v0 offset:2048
	ds_read_b128 v[166:169], v0 offset:3072
	v_mov_b32_e32 v0, v34
	ds_read_b128 v[170:173], v39
	ds_read_b128 v[174:177], v39 offset:1024
	ds_read_b128 v[178:181], v39 offset:2048
	ds_read_b128 v[182:185], v39 offset:3072
	ds_read_b128 v[186:189], v39 offset:4096
	ds_read_b128 v[190:193], v39 offset:5120
	ds_read_b128 v[194:197], v39 offset:6144
	ds_read_b128 v[198:201], v39 offset:7168
	s_add_i32 m0, s85, 0xc000
	v_lshl_add_u64 v[40:41], s[26:27], 0, v[0:1]
	v_lshl_add_u64 v[40:41], v[40:41], 0, s[64:65]
	v_mov_b32_e32 v0, v36
	global_load_lds_dwordx4 v[40:41], off
	s_add_i32 m0, s85, 0xe000
	v_lshl_add_u64 v[40:41], s[26:27], 0, v[0:1]
	v_lshl_add_u64 v[40:41], v[40:41], 0, s[64:65]
	global_load_lds_dwordx4 v[40:41], off
	s_waitcnt vmcnt(8)
	s_waitcnt lgkmcnt(0)
	s_barrier
	s_setprio 1
	s_waitcnt lgkmcnt(0)
	v_mfma_i32_16x16x64_i8 v[134:137], v[138:141], v[170:173], v[134:137]
	v_mfma_i32_16x16x64_i8 v[130:133], v[146:149], v[170:173], v[130:133]
	v_mfma_i32_16x16x64_i8 v[126:129], v[138:141], v[178:181], v[126:129]
	v_mfma_i32_16x16x64_i8 v[122:125], v[146:149], v[178:181], v[122:125]
	v_mfma_i32_16x16x64_i8 v[118:121], v[138:141], v[186:189], v[118:121]
	v_mfma_i32_16x16x64_i8 v[114:117], v[146:149], v[186:189], v[114:117]
	v_mfma_i32_16x16x64_i8 v[110:113], v[138:141], v[194:197], v[110:113]
	v_mfma_i32_16x16x64_i8 v[106:109], v[146:149], v[194:197], v[106:109]
	v_mfma_i32_16x16x64_i8 v[134:137], v[142:145], v[174:177], v[134:137]
	v_mfma_i32_16x16x64_i8 v[130:133], v[150:153], v[174:177], v[130:133]
	v_mfma_i32_16x16x64_i8 v[126:129], v[142:145], v[182:185], v[126:129]
	v_mfma_i32_16x16x64_i8 v[122:125], v[150:153], v[182:185], v[122:125]
	v_mfma_i32_16x16x64_i8 v[118:121], v[142:145], v[190:193], v[118:121]
	v_mfma_i32_16x16x64_i8 v[114:117], v[150:153], v[190:193], v[114:117]
	v_mfma_i32_16x16x64_i8 v[110:113], v[142:145], v[198:201], v[110:113]
	v_mfma_i32_16x16x64_i8 v[106:109], v[150:153], v[198:201], v[106:109]
	s_setprio 0
	s_setprio 1
	v_mfma_i32_16x16x64_i8 v[78:81], v[154:157], v[170:173], v[78:81]
	v_mfma_i32_16x16x64_i8 v[74:77], v[162:165], v[170:173], v[74:77]
	v_mfma_i32_16x16x64_i8 v[62:65], v[154:157], v[178:181], v[62:65]
	v_mfma_i32_16x16x64_i8 v[58:61], v[162:165], v[178:181], v[58:61]
	v_mfma_i32_16x16x64_i8 v[54:57], v[154:157], v[186:189], v[54:57]
	v_mfma_i32_16x16x64_i8 v[50:53], v[162:165], v[186:189], v[50:53]
	v_mfma_i32_16x16x64_i8 v[46:49], v[154:157], v[194:197], v[46:49]
	v_mfma_i32_16x16x64_i8 v[40:43], v[162:165], v[194:197], v[42:45]
	v_mfma_i32_16x16x64_i8 v[78:81], v[158:161], v[174:177], v[78:81]
	v_mfma_i32_16x16x64_i8 v[74:77], v[166:169], v[174:177], v[74:77]
	v_mfma_i32_16x16x64_i8 v[62:65], v[158:161], v[182:185], v[62:65]
	v_mfma_i32_16x16x64_i8 v[58:61], v[166:169], v[182:185], v[58:61]
	v_mfma_i32_16x16x64_i8 v[54:57], v[158:161], v[190:193], v[54:57]
	v_mfma_i32_16x16x64_i8 v[50:53], v[166:169], v[190:193], v[50:53]
	v_mfma_i32_16x16x64_i8 v[46:49], v[158:161], v[198:201], v[46:49]
	v_mfma_i32_16x16x64_i8 v[40:43], v[166:169], v[198:201], v[40:43]
	s_setprio 0
	s_barrier
	s_add_i32 s26, s28, s33
	ds_read_b128 v[170:173], v39 offset:16384
	ds_read_b128 v[174:177], v39 offset:17408
	ds_read_b128 v[178:181], v39 offset:18432
	ds_read_b128 v[182:185], v39 offset:19456
	ds_read_b128 v[186:189], v39 offset:20480
	ds_read_b128 v[190:193], v39 offset:21504
	ds_read_b128 v[194:197], v39 offset:22528
	ds_read_b128 v[198:201], v39 offset:23552
	s_mov_b32 m0, s26
	s_nop 0
	global_load_lds_dwordx4 v35, s[14:15]
	s_add_i32 m0, s26, 0x2000
	s_add_u32 s26, s14, 0x20000
	global_load_lds_dwordx4 v37, s[14:15]
	s_addc_u32 s27, s15, 0
	s_add_i32 s28, s29, s33
	s_mov_b32 m0, s28
	s_nop 0
	global_load_lds_dwordx4 v35, s[26:27]
	s_add_i32 m0, s28, 0x2000
	s_nop 0
	global_load_lds_dwordx4 v37, s[26:27]
	s_waitcnt vmcnt(6)
	s_waitcnt lgkmcnt(0)
	s_barrier
	s_setprio 1
	s_waitcnt lgkmcnt(0)
	v_mfma_i32_16x16x64_i8 v[102:105], v[138:141], v[170:173], v[102:105]
	v_mfma_i32_16x16x64_i8 v[98:101], v[146:149], v[170:173], v[98:101]
	v_mfma_i32_16x16x64_i8 v[94:97], v[138:141], v[178:181], v[94:97]
	v_mfma_i32_16x16x64_i8 v[90:93], v[146:149], v[178:181], v[90:93]
	v_mfma_i32_16x16x64_i8 v[86:89], v[138:141], v[186:189], v[86:89]
	v_mfma_i32_16x16x64_i8 v[82:85], v[146:149], v[186:189], v[82:85]
	v_mfma_i32_16x16x64_i8 v[70:73], v[138:141], v[194:197], v[70:73]
	v_mfma_i32_16x16x64_i8 v[66:69], v[146:149], v[194:197], v[66:69]
	v_mfma_i32_16x16x64_i8 v[102:105], v[142:145], v[174:177], v[102:105]
	v_mfma_i32_16x16x64_i8 v[98:101], v[150:153], v[174:177], v[98:101]
	v_mfma_i32_16x16x64_i8 v[94:97], v[142:145], v[182:185], v[94:97]
	v_mfma_i32_16x16x64_i8 v[90:93], v[150:153], v[182:185], v[90:93]
	v_mfma_i32_16x16x64_i8 v[86:89], v[142:145], v[190:193], v[86:89]
	v_mfma_i32_16x16x64_i8 v[82:85], v[150:153], v[190:193], v[82:85]
	v_mfma_i32_16x16x64_i8 v[70:73], v[142:145], v[198:201], v[70:73]
	v_mfma_i32_16x16x64_i8 v[66:69], v[150:153], v[198:201], v[66:69]
	s_setprio 0
	s_setprio 1
	v_mfma_i32_16x16x64_i8 v[30:33], v[154:157], v[170:173], v[30:33]
	v_mfma_i32_16x16x64_i8 v[26:29], v[162:165], v[170:173], v[26:29]
	v_mfma_i32_16x16x64_i8 v[22:25], v[154:157], v[178:181], v[22:25]
	v_mfma_i32_16x16x64_i8 v[18:21], v[162:165], v[178:181], v[18:21]
	v_mfma_i32_16x16x64_i8 v[14:17], v[154:157], v[186:189], v[14:17]
	v_mfma_i32_16x16x64_i8 v[10:13], v[162:165], v[186:189], v[10:13]
	v_mfma_i32_16x16x64_i8 v[6:9], v[154:157], v[194:197], v[6:9]
	v_mfma_i32_16x16x64_i8 v[2:5], v[162:165], v[194:197], v[2:5]
	v_mfma_i32_16x16x64_i8 v[30:33], v[158:161], v[174:177], v[30:33]
	v_mfma_i32_16x16x64_i8 v[26:29], v[166:169], v[174:177], v[26:29]
	v_mfma_i32_16x16x64_i8 v[22:25], v[158:161], v[182:185], v[22:25]
	v_mfma_i32_16x16x64_i8 v[18:21], v[166:169], v[182:185], v[18:21]
	v_mfma_i32_16x16x64_i8 v[14:17], v[158:161], v[190:193], v[14:17]
	v_mfma_i32_16x16x64_i8 v[10:13], v[166:169], v[190:193], v[10:13]
	v_mfma_i32_16x16x64_i8 v[6:9], v[158:161], v[198:201], v[6:9]
	v_mfma_i32_16x16x64_i8 v[2:5], v[166:169], v[198:201], v[2:5]
	s_setprio 0
	s_barrier
	s_add_i32 s28, 0, 0x18000
	v_add_u32_e32 v0, s28, v38
	s_add_i32 s29, 0, 0x1c000
	ds_read_b128 v[138:141], v0
	ds_read_b128 v[142:145], v0 offset:1024
	ds_read_b128 v[146:149], v0 offset:2048
	ds_read_b128 v[150:153], v0 offset:3072
	v_add_u32_e32 v0, s29, v38
	ds_read_b128 v[154:157], v0
	ds_read_b128 v[158:161], v0 offset:1024
	ds_read_b128 v[162:165], v0 offset:2048
	ds_read_b128 v[166:169], v0 offset:3072
	s_add_u32 s26, s12, 0x20000
	ds_read_b128 v[170:173], v39 offset:32768
	ds_read_b128 v[174:177], v39 offset:33792
	ds_read_b128 v[178:181], v39 offset:34816
	ds_read_b128 v[182:185], v39 offset:35840
	ds_read_b128 v[186:189], v39 offset:36864
	ds_read_b128 v[190:193], v39 offset:37888
	ds_read_b128 v[194:197], v39 offset:38912
	ds_read_b128 v[198:201], v39 offset:39936
	s_addc_u32 s27, s13, 0
	s_mov_b32 m0, s85
	s_nop 0
	global_load_lds_dwordx4 v34, s[12:13]
	s_mov_b32 m0, s3
	s_nop 0
	global_load_lds_dwordx4 v36, s[12:13]
	s_mov_b32 m0, s17
	s_nop 0
	global_load_lds_dwordx4 v34, s[26:27]
	s_mov_b32 m0, s18
	s_nop 0
	global_load_lds_dwordx4 v36, s[26:27]
	s_waitcnt vmcnt(8)
	s_waitcnt lgkmcnt(0)
	s_barrier
	s_setprio 1
	s_waitcnt lgkmcnt(0)
	v_mfma_i32_16x16x64_i8 v[134:137], v[138:141], v[170:173], v[134:137]
	v_mfma_i32_16x16x64_i8 v[130:133], v[146:149], v[170:173], v[130:133]
	v_mfma_i32_16x16x64_i8 v[126:129], v[138:141], v[178:181], v[126:129]
	v_mfma_i32_16x16x64_i8 v[122:125], v[146:149], v[178:181], v[122:125]
	v_mfma_i32_16x16x64_i8 v[118:121], v[138:141], v[186:189], v[118:121]
	v_mfma_i32_16x16x64_i8 v[114:117], v[146:149], v[186:189], v[114:117]
	v_mfma_i32_16x16x64_i8 v[110:113], v[138:141], v[194:197], v[110:113]
	v_mfma_i32_16x16x64_i8 v[106:109], v[146:149], v[194:197], v[106:109]
	v_mfma_i32_16x16x64_i8 v[134:137], v[142:145], v[174:177], v[134:137]
	v_mfma_i32_16x16x64_i8 v[130:133], v[150:153], v[174:177], v[130:133]
	v_mfma_i32_16x16x64_i8 v[126:129], v[142:145], v[182:185], v[126:129]
	v_mfma_i32_16x16x64_i8 v[122:125], v[150:153], v[182:185], v[122:125]
	v_mfma_i32_16x16x64_i8 v[118:121], v[142:145], v[190:193], v[118:121]
	v_mfma_i32_16x16x64_i8 v[114:117], v[150:153], v[190:193], v[114:117]
	v_mfma_i32_16x16x64_i8 v[110:113], v[142:145], v[198:201], v[110:113]
	v_mfma_i32_16x16x64_i8 v[106:109], v[150:153], v[198:201], v[106:109]
	s_setprio 0
	s_setprio 1
	v_mfma_i32_16x16x64_i8 v[78:81], v[154:157], v[170:173], v[78:81]
	v_mfma_i32_16x16x64_i8 v[74:77], v[162:165], v[170:173], v[74:77]
	v_mfma_i32_16x16x64_i8 v[62:65], v[154:157], v[178:181], v[62:65]
	v_mfma_i32_16x16x64_i8 v[58:61], v[162:165], v[178:181], v[58:61]
	v_mfma_i32_16x16x64_i8 v[54:57], v[154:157], v[186:189], v[54:57]
	v_mfma_i32_16x16x64_i8 v[50:53], v[162:165], v[186:189], v[50:53]
	v_mfma_i32_16x16x64_i8 v[44:47], v[154:157], v[194:197], v[46:49]
	v_mfma_i32_16x16x64_i8 v[40:43], v[162:165], v[194:197], v[40:43]
	v_mfma_i32_16x16x64_i8 v[78:81], v[158:161], v[174:177], v[78:81]
	v_mfma_i32_16x16x64_i8 v[74:77], v[166:169], v[174:177], v[74:77]
	v_mfma_i32_16x16x64_i8 v[62:65], v[158:161], v[182:185], v[62:65]
	v_mfma_i32_16x16x64_i8 v[58:61], v[166:169], v[182:185], v[58:61]
	v_mfma_i32_16x16x64_i8 v[54:57], v[158:161], v[190:193], v[54:57]
	v_mfma_i32_16x16x64_i8 v[50:53], v[166:169], v[190:193], v[50:53]
	v_mfma_i32_16x16x64_i8 v[46:49], v[158:161], v[198:201], v[44:47]
	v_mfma_i32_16x16x64_i8 v[42:45], v[166:169], v[198:201], v[40:43]
	s_setprio 0
	s_barrier
	v_mov_b32_e32 v0, v35
	ds_read_b128 v[170:173], v39 offset:49152
	ds_read_b128 v[174:177], v39 offset:50176
	ds_read_b128 v[178:181], v39 offset:51200
	ds_read_b128 v[182:185], v39 offset:52224
	ds_read_b128 v[186:189], v39 offset:53248
	ds_read_b128 v[190:193], v39 offset:54272
	ds_read_b128 v[194:197], v39 offset:55296
	ds_read_b128 v[198:201], v39 offset:56320
	s_add_i32 s26, s28, s33
	v_lshl_add_u64 v[40:41], s[14:15], 0, v[0:1]
	v_lshl_add_u64 v[40:41], v[40:41], 0, s[90:91]
	s_mov_b32 m0, s26
	v_mov_b32_e32 v0, v37
	global_load_lds_dwordx4 v[40:41], off
	s_add_i32 m0, s26, 0x2000
	s_nop 0
	v_lshl_add_u64 v[40:41], s[14:15], 0, v[0:1]
	s_add_u32 s14, s14, 0x20080
	v_lshl_add_u64 v[40:41], v[40:41], 0, s[90:91]
	s_addc_u32 s15, s15, 0
	s_add_i32 s26, s29, s33
	global_load_lds_dwordx4 v[40:41], off
	s_mov_b32 m0, s26
	s_nop 0
	global_load_lds_dwordx4 v35, s[14:15]
	s_add_i32 m0, s26, 0x2000
	s_nop 0
	global_load_lds_dwordx4 v37, s[14:15]
	s_waitcnt vmcnt(6)
	s_waitcnt lgkmcnt(0)
	s_barrier
	s_setprio 1
	s_waitcnt lgkmcnt(0)
	v_mfma_i32_16x16x64_i8 v[102:105], v[138:141], v[170:173], v[102:105]
	v_mfma_i32_16x16x64_i8 v[98:101], v[146:149], v[170:173], v[98:101]
	v_mfma_i32_16x16x64_i8 v[94:97], v[138:141], v[178:181], v[94:97]
	v_mfma_i32_16x16x64_i8 v[90:93], v[146:149], v[178:181], v[90:93]
	v_mfma_i32_16x16x64_i8 v[86:89], v[138:141], v[186:189], v[86:89]
	v_mfma_i32_16x16x64_i8 v[82:85], v[146:149], v[186:189], v[82:85]
	v_mfma_i32_16x16x64_i8 v[70:73], v[138:141], v[194:197], v[70:73]
	v_mfma_i32_16x16x64_i8 v[66:69], v[146:149], v[194:197], v[66:69]
	v_mfma_i32_16x16x64_i8 v[102:105], v[142:145], v[174:177], v[102:105]
	v_mfma_i32_16x16x64_i8 v[98:101], v[150:153], v[174:177], v[98:101]
	v_mfma_i32_16x16x64_i8 v[94:97], v[142:145], v[182:185], v[94:97]
	v_mfma_i32_16x16x64_i8 v[90:93], v[150:153], v[182:185], v[90:93]
	v_mfma_i32_16x16x64_i8 v[86:89], v[142:145], v[190:193], v[86:89]
	v_mfma_i32_16x16x64_i8 v[82:85], v[150:153], v[190:193], v[82:85]
	v_mfma_i32_16x16x64_i8 v[70:73], v[142:145], v[198:201], v[70:73]
	v_mfma_i32_16x16x64_i8 v[66:69], v[150:153], v[198:201], v[66:69]
	s_setprio 0
	s_setprio 1
	v_mfma_i32_16x16x64_i8 v[30:33], v[154:157], v[170:173], v[30:33]
	v_mfma_i32_16x16x64_i8 v[26:29], v[162:165], v[170:173], v[26:29]
	v_mfma_i32_16x16x64_i8 v[22:25], v[154:157], v[178:181], v[22:25]
	v_mfma_i32_16x16x64_i8 v[18:21], v[162:165], v[178:181], v[18:21]
	v_mfma_i32_16x16x64_i8 v[14:17], v[154:157], v[186:189], v[14:17]
	v_mfma_i32_16x16x64_i8 v[10:13], v[162:165], v[186:189], v[10:13]
	v_mfma_i32_16x16x64_i8 v[6:9], v[154:157], v[194:197], v[6:9]
	v_mfma_i32_16x16x64_i8 v[2:5], v[162:165], v[194:197], v[2:5]
	v_mfma_i32_16x16x64_i8 v[30:33], v[158:161], v[174:177], v[30:33]
	v_mfma_i32_16x16x64_i8 v[26:29], v[166:169], v[174:177], v[26:29]
	v_mfma_i32_16x16x64_i8 v[22:25], v[158:161], v[182:185], v[22:25]
	v_mfma_i32_16x16x64_i8 v[18:21], v[166:169], v[182:185], v[18:21]
	v_mfma_i32_16x16x64_i8 v[14:17], v[158:161], v[190:193], v[14:17]
	v_mfma_i32_16x16x64_i8 v[10:13], v[166:169], v[190:193], v[10:13]
	v_mfma_i32_16x16x64_i8 v[6:9], v[158:161], v[198:201], v[6:9]
	v_mfma_i32_16x16x64_i8 v[2:5], v[166:169], v[198:201], v[2:5]
	s_setprio 0
	s_barrier
	v_mov_b32_e32 v0, v34
	s_mov_b32 m0, s19
	v_lshl_add_u64 v[40:41], s[12:13], 0, v[0:1]
	v_lshl_add_u64 v[40:41], v[40:41], 0, s[90:91]
	v_mov_b32_e32 v0, v36
	global_load_lds_dwordx4 v[40:41], off
	s_mov_b32 m0, s20
	v_lshl_add_u64 v[40:41], s[12:13], 0, v[0:1]
	v_lshl_add_u64 v[40:41], v[40:41], 0, s[90:91]
	global_load_lds_dwordx4 v[40:41], off
	s_add_i32 s25, s25, 2
	s_add_u32 s10, s10, 0x100
	s_addc_u32 s11, s11, 0
	s_cmp_gt_u32 s25, 5
	s_cbranch_scc0 .LBB0_689
	s_add_u32 s17, s0, 0x400000
	s_addc_u32 s15, s1, 0
	s_add_u32 s6, s0, 0x680000
	s_addc_u32 s7, s1, 0
	s_lshl_b64 s[8:9], s[94:95], 2
	s_add_u32 s8, s0, s8
	s_addc_u32 s9, s1, s9
	s_lshl_b32 s16, s16, 8
	v_mbcnt_lo_u32_b32 v0, -1, 0
	v_mbcnt_hi_u32_b32 v0, -1, v0
	s_lshl_b32 s2, s2, 8
	v_bfe_u32 v169, v0, 4, 2
	s_or_b32 s14, s16, s72
	v_lshlrev_b32_e32 v149, 3, v169
	s_add_i32 s2, s2, s87
	v_or_b32_e32 v153, s14, v149
	v_and_or_b32 v186, v0, 15, s2
	v_lshlrev_b32_e32 v0, 2, v153
	v_lshl_add_u64 v[138:139], s[8:9], 0, v[0:1]
	s_mov_b64 s[2:3], 0x764000
	v_lshl_add_u64 v[170:171], v[138:139], 0, s[2:3]
	s_mov_b32 s2, 0x764000
	v_add_co_u32_e32 v138, vcc, s2, v138
	v_or_b32_e32 v178, 16, v186
	s_nop 0
	v_addc_co_u32_e32 v139, vcc, 0, v139, vcc
	global_load_dwordx4 v[142:145], v[138:139], off
	s_nop 0
	global_load_dwordx4 v[138:141], v[170:171], off offset:16
	v_or_b32_e32 v172, 32, v186
	v_or_b32_e32 v164, 48, v186
	v_add_u32_e32 v158, 0x80, v186
	v_add_u32_e32 v154, 0x90, v186
	v_ashrrev_i32_e32 v187, 31, v186
	v_ashrrev_i32_e32 v179, 31, v178
	v_ashrrev_i32_e32 v173, 31, v172
	v_ashrrev_i32_e32 v165, 31, v164
	v_ashrrev_i32_e32 v159, 31, v158
	v_ashrrev_i32_e32 v155, 31, v154
	v_add_u32_e32 v150, 0xa0, v186
	v_add_u32_e32 v146, 0xb0, v186
	v_lshl_add_u64 v[34:35], v[178:179], 2, s[6:7]
	v_lshl_add_u64 v[36:37], v[172:173], 2, s[6:7]
	v_lshl_add_u64 v[38:39], v[164:165], 2, s[6:7]
	v_lshl_add_u64 v[40:41], v[158:159], 2, s[6:7]
	v_lshl_add_u64 v[156:157], v[154:155], 2, s[6:7]
	v_ashrrev_i32_e32 v151, 31, v150
	v_ashrrev_i32_e32 v147, 31, v146
	v_lshl_add_u64 v[162:163], v[186:187], 2, s[6:7]
	v_lshl_add_u64 v[160:161], v[150:151], 2, s[6:7]
	v_lshl_add_u64 v[166:167], v[146:147], 2, s[6:7]
	global_load_dword v190, v[162:163], off
	global_load_dword v182, v[34:35], off
	global_load_dword v176, v[36:37], off
	global_load_dword v168, v[38:39], off
	s_nop 0
	global_load_dword v162, v[40:41], off
	s_nop 0
	global_load_dword v156, v[156:157], off
	s_nop 0
	global_load_dword v152, v[160:161], off
	global_load_dword v148, v[166:167], off
	global_load_dwordx4 v[34:37], v[170:171], off offset:528
	global_load_dwordx4 v[38:41], v[170:171], off offset:512
	v_readlane_b32 vcc_lo, v254, 19
	v_readlane_b32 vcc_hi, v254, 20
	s_and_b64 vcc, exec, vcc
	s_cbranch_vccz .LBB0_692
	s_barrier
.LBB0_692:
	s_add_i32 s8, s16, 0xfffffa00
	v_cvt_f32_i32_e32 v135, v135
	v_cvt_f32_i32_e32 v134, v134
	v_cvt_f32_i32_e32 v137, v137
	v_cvt_f32_i32_e32 v136, v136
	v_cvt_f32_i32_e32 v131, v131
	v_cvt_f32_i32_e32 v130, v130
	v_cvt_f32_i32_e32 v133, v133
	v_cvt_f32_i32_e32 v132, v132
	s_cmpk_lt_u32 s8, 0x280
	s_cselect_b64 s[12:13], -1, 0
	s_add_i32 s2, s14, 0xfffffa00
	s_lshr_b32 s2, s2, 3
	s_add_u32 s2, s17, s2
	s_addc_u32 s3, s15, 0
	v_cmp_eq_u32_e64 s[6:7], 0, v169
	s_cmpk_gt_u32 s8, 0x27f
	s_mov_b64 s[64:65], 0x1f040080
	s_waitcnt vmcnt(0)
	v_pk_mul_f32 v[136:137], v[144:145], v[136:137]
	v_pk_mul_f32 v[134:135], v[142:143], v[134:135]
	v_pk_mul_f32 v[160:161], v[140:141], v[132:133]
	v_pk_mul_f32 v[130:131], v[138:139], v[130:131]
	v_pk_mul_f32 v[132:133], v[136:137], v[190:191] op_sel_hi:[1,0]
	v_pk_mul_f32 v[134:135], v[134:135], v[190:191] op_sel_hi:[1,0]
	v_pk_mul_f32 v[136:137], v[130:131], v[190:191] op_sel_hi:[1,0]
	v_pk_mul_f32 v[130:131], v[160:161], v[190:191] op_sel_hi:[1,0]
	s_cbranch_scc1 .LBB0_696
	v_mul_f32_e32 v0, v135, v135
	v_mul_f32_e32 v157, v133, v133
	v_fmac_f32_e32 v0, v134, v134
	v_fmac_f32_e32 v157, v132, v132
	v_add_f32_e32 v0, v0, v157
	v_mul_f32_e32 v157, v137, v137
	v_fmac_f32_e32 v157, v136, v136
	v_add_f32_e32 v0, v157, v0
	v_mul_f32_e32 v157, v131, v131
	v_fmac_f32_e32 v157, v130, v130
	v_add_f32_e32 v0, v157, v0
	ds_swizzle_b32 v157, v0 offset:swizzle(SWAP,16)
	s_waitcnt lgkmcnt(0)
	v_add_f32_e32 v0, v0, v157
	v_mov_b32_e32 v157, v0
	s_nop 1
	v_permlane32_swap_b32_e32 v0, v157
	s_and_saveexec_b64 s[8:9], s[6:7]
	s_cbranch_execz .LBB0_695
	v_mov_b64_e32 v[160:161], s[2:3]
	s_movk_i32 s10, 0x50
	v_add_f32_e32 v0, v0, v157
	v_mad_i64_i32 v[160:161], s[10:11], v186, s10, v[160:161]
	global_store_dword v[160:161], v0, off

.LBB0_918:
	s_add_u32 s30, s14, s28
	s_addc_u32 s31, s15, s29
	s_add_u32 s34, s30, 0x100
	s_addc_u32 s35, s31, 0
	s_and_b64 s[24:25], s[26:27], exec
	s_cselect_b32 s25, s11, s35
	s_cselect_b32 s24, s10, s34
	s_add_u32 s28, s20, s28
	s_addc_u32 s29, s21, s29
	s_add_u32 s28, s28, 0x100
	s_addc_u32 s29, s29, 0
	s_and_b64 s[26:27], s[26:27], exec
	v_add_u32_e32 v0, s43, v151
	s_cselect_b32 s27, s59, s29
	s_cselect_b32 s26, s65, s28
	s_add_u32 s36, s30, 0x90080
	ds_read_b128 v[130:133], v0
	ds_read_b128 v[134:137], v0 offset:1024
	ds_read_b128 v[154:157], v0 offset:2048
	ds_read_b128 v[158:161], v0 offset:3072
	v_add_u32_e32 v0, s44, v151
	s_addc_u32 s37, s31, 0
	ds_read_b128 v[162:165], v0
	ds_read_b128 v[166:169], v0 offset:1024
	ds_read_b128 v[170:173], v0 offset:2048
	ds_read_b128 v[174:177], v0 offset:3072
	s_add_u32 s34, s26, 0x10000
	s_addc_u32 s35, s27, 0
	s_add_u32 s30, s24, 0x90000
	s_addc_u32 s31, s25, 0
	s_add_u32 s28, s26, 0x10080
	s_addc_u32 s29, s27, 0
	s_mov_b32 m0, s45
	ds_read_b128 v[178:181], v152
	ds_read_b128 v[182:185], v152 offset:1024
	ds_read_b128 v[186:189], v152 offset:2048
	ds_read_b128 v[190:193], v152 offset:3072
	ds_read_b128 v[194:197], v152 offset:4096
	ds_read_b128 v[198:201], v152 offset:5120
	ds_read_b128 v[202:205], v152 offset:6144
	ds_read_b128 v[206:209], v152 offset:7168
	s_nop 0
	global_load_lds_dwordx4 v141, s[36:37]
	s_mov_b32 m0, s46
	s_nop 0
	global_load_lds_dwordx4 v149, s[36:37]
	s_waitcnt vmcnt(8)
	s_waitcnt lgkmcnt(0)
	s_barrier
	s_setprio 1
	s_waitcnt lgkmcnt(0)
	v_mfma_f32_16x16x32_bf16 v[126:129], v[130:133], v[178:181], v[126:129]
	v_mfma_f32_16x16x32_bf16 v[122:125], v[154:157], v[178:181], v[122:125]
	v_mfma_f32_16x16x32_bf16 v[118:121], v[130:133], v[186:189], v[118:121]
	v_mfma_f32_16x16x32_bf16 v[110:113], v[154:157], v[186:189], v[110:113]
	v_mfma_f32_16x16x32_bf16 v[102:105], v[130:133], v[194:197], v[102:105]
	v_mfma_f32_16x16x32_bf16 v[94:97], v[154:157], v[194:197], v[94:97]
	v_mfma_f32_16x16x32_bf16 v[86:89], v[130:133], v[202:205], v[86:89]
	v_mfma_f32_16x16x32_bf16 v[78:81], v[154:157], v[202:205], v[78:81]
	v_mfma_f32_16x16x32_bf16 v[126:129], v[134:137], v[182:185], v[126:129]
	v_mfma_f32_16x16x32_bf16 v[122:125], v[158:161], v[182:185], v[122:125]
	v_mfma_f32_16x16x32_bf16 v[118:121], v[134:137], v[190:193], v[118:121]
	v_mfma_f32_16x16x32_bf16 v[110:113], v[158:161], v[190:193], v[110:113]
	v_mfma_f32_16x16x32_bf16 v[102:105], v[134:137], v[198:201], v[102:105]
	v_mfma_f32_16x16x32_bf16 v[94:97], v[158:161], v[198:201], v[94:97]
	v_mfma_f32_16x16x32_bf16 v[86:89], v[134:137], v[206:209], v[86:89]
	v_mfma_f32_16x16x32_bf16 v[78:81], v[158:161], v[206:209], v[78:81]
	s_setprio 0
	s_setprio 1
	v_mfma_f32_16x16x32_bf16 v[114:117], v[162:165], v[178:181], v[114:117]
	v_mfma_f32_16x16x32_bf16 v[106:109], v[170:173], v[178:181], v[106:109]
	v_mfma_f32_16x16x32_bf16 v[98:101], v[162:165], v[186:189], v[98:101]
	v_mfma_f32_16x16x32_bf16 v[90:93], v[170:173], v[186:189], v[90:93]
	v_mfma_f32_16x16x32_bf16 v[82:85], v[162:165], v[194:197], v[82:85]
	v_mfma_f32_16x16x32_bf16 v[74:77], v[170:173], v[194:197], v[74:77]
	v_mfma_f32_16x16x32_bf16 v[70:73], v[162:165], v[202:205], v[70:73]
	v_mfma_f32_16x16x32_bf16 v[66:69], v[170:173], v[202:205], v[66:69]
	v_mfma_f32_16x16x32_bf16 v[114:117], v[166:169], v[182:185], v[114:117]
	v_mfma_f32_16x16x32_bf16 v[106:109], v[174:177], v[182:185], v[106:109]
	v_mfma_f32_16x16x32_bf16 v[98:101], v[166:169], v[190:193], v[98:101]
	v_mfma_f32_16x16x32_bf16 v[90:93], v[174:177], v[190:193], v[90:93]
	v_mfma_f32_16x16x32_bf16 v[82:85], v[166:169], v[198:201], v[82:85]
	v_mfma_f32_16x16x32_bf16 v[74:77], v[174:177], v[198:201], v[74:77]
	v_mfma_f32_16x16x32_bf16 v[70:73], v[166:169], v[206:209], v[70:73]
	v_mfma_f32_16x16x32_bf16 v[66:69], v[174:177], v[206:209], v[66:69]
	s_setprio 0
	s_barrier
	s_mov_b32 m0, s47
	ds_read_b128 v[178:181], v152 offset:16384
	ds_read_b128 v[182:185], v152 offset:17408
	ds_read_b128 v[186:189], v152 offset:18432
	ds_read_b128 v[190:193], v152 offset:19456
	ds_read_b128 v[194:197], v152 offset:20480
	ds_read_b128 v[198:201], v152 offset:21504
	ds_read_b128 v[202:205], v152 offset:22528
	ds_read_b128 v[206:209], v152 offset:23552
	s_nop 0
	global_load_lds_dwordx4 v145, s[26:27]
	s_mov_b32 m0, s48
	s_nop 0
	global_load_lds_dwordx4 v150, s[26:27]
	s_mov_b32 m0, s49
	s_nop 0
	global_load_lds_dwordx4 v145, s[34:35]
	s_mov_b32 m0, s50
	s_nop 0
	global_load_lds_dwordx4 v150, s[34:35]
	s_mov_b32 m0, s85
	s_nop 0
	global_load_lds_dwordx4 v141, s[24:25]
	s_mov_b32 m0, s38
	s_nop 0
	global_load_lds_dwordx4 v149, s[24:25]
	s_waitcnt vmcnt(8)
	s_waitcnt lgkmcnt(0)
	s_barrier
	s_setprio 1
	s_waitcnt lgkmcnt(0)
	v_mfma_f32_16x16x32_bf16 v[62:65], v[130:133], v[178:181], v[62:65]
	v_mfma_f32_16x16x32_bf16 v[58:61], v[154:157], v[178:181], v[58:61]
	v_mfma_f32_16x16x32_bf16 v[54:57], v[130:133], v[186:189], v[54:57]
	v_mfma_f32_16x16x32_bf16 v[46:49], v[154:157], v[186:189], v[46:49]
	v_mfma_f32_16x16x32_bf16 v[38:41], v[130:133], v[194:197], v[38:41]
	v_mfma_f32_16x16x32_bf16 v[30:33], v[154:157], v[194:197], v[30:33]
	v_mfma_f32_16x16x32_bf16 v[22:25], v[130:133], v[202:205], v[22:25]
	v_mfma_f32_16x16x32_bf16 v[14:17], v[154:157], v[202:205], v[14:17]
	v_mfma_f32_16x16x32_bf16 v[62:65], v[134:137], v[182:185], v[62:65]
	v_mfma_f32_16x16x32_bf16 v[58:61], v[158:161], v[182:185], v[58:61]
	v_mfma_f32_16x16x32_bf16 v[54:57], v[134:137], v[190:193], v[54:57]
	v_mfma_f32_16x16x32_bf16 v[46:49], v[158:161], v[190:193], v[46:49]
	v_mfma_f32_16x16x32_bf16 v[38:41], v[134:137], v[198:201], v[38:41]
	v_mfma_f32_16x16x32_bf16 v[30:33], v[158:161], v[198:201], v[30:33]
	v_mfma_f32_16x16x32_bf16 v[22:25], v[134:137], v[206:209], v[22:25]
	v_mfma_f32_16x16x32_bf16 v[14:17], v[158:161], v[206:209], v[14:17]
	s_setprio 0
	s_setprio 1
	v_mfma_f32_16x16x32_bf16 v[50:53], v[162:165], v[178:181], v[50:53]
	v_mfma_f32_16x16x32_bf16 v[42:45], v[170:173], v[178:181], v[42:45]
	v_mfma_f32_16x16x32_bf16 v[34:37], v[162:165], v[186:189], v[34:37]
	v_mfma_f32_16x16x32_bf16 v[26:29], v[170:173], v[186:189], v[26:29]
	v_mfma_f32_16x16x32_bf16 v[18:21], v[162:165], v[194:197], v[18:21]
	v_mfma_f32_16x16x32_bf16 v[10:13], v[170:173], v[194:197], v[10:13]
	v_mfma_f32_16x16x32_bf16 v[6:9], v[162:165], v[202:205], v[6:9]
	v_mfma_f32_16x16x32_bf16 v[2:5], v[170:173], v[202:205], v[2:5]
	v_mfma_f32_16x16x32_bf16 v[50:53], v[166:169], v[182:185], v[50:53]
	v_mfma_f32_16x16x32_bf16 v[42:45], v[174:177], v[182:185], v[42:45]
	v_mfma_f32_16x16x32_bf16 v[34:37], v[166:169], v[190:193], v[34:37]
	v_mfma_f32_16x16x32_bf16 v[26:29], v[174:177], v[190:193], v[26:29]
	v_mfma_f32_16x16x32_bf16 v[18:21], v[166:169], v[198:201], v[18:21]
	v_mfma_f32_16x16x32_bf16 v[10:13], v[174:177], v[198:201], v[10:13]
	v_mfma_f32_16x16x32_bf16 v[6:9], v[166:169], v[206:209], v[6:9]
	v_mfma_f32_16x16x32_bf16 v[2:5], v[174:177], v[206:209], v[2:5]
	s_setprio 0
	s_barrier
	v_add_u32_e32 v0, s51, v151
	ds_read_b128 v[130:133], v0
	ds_read_b128 v[134:137], v0 offset:1024
	ds_read_b128 v[154:157], v0 offset:2048
	ds_read_b128 v[158:161], v0 offset:3072
	v_add_u32_e32 v0, s52, v151
	ds_read_b128 v[162:165], v0
	ds_read_b128 v[166:169], v0 offset:1024
	ds_read_b128 v[170:173], v0 offset:2048
	ds_read_b128 v[174:177], v0 offset:3072
	s_mov_b32 m0, s39
	ds_read_b128 v[178:181], v152 offset:32768
	ds_read_b128 v[182:185], v152 offset:33792
	ds_read_b128 v[186:189], v152 offset:34816
	ds_read_b128 v[190:193], v152 offset:35840
	ds_read_b128 v[194:197], v152 offset:36864
	ds_read_b128 v[198:201], v152 offset:37888
	ds_read_b128 v[202:205], v152 offset:38912
	ds_read_b128 v[206:209], v152 offset:39936
	s_nop 0
	global_load_lds_dwordx4 v141, s[30:31]
	s_mov_b32 m0, s40
	s_nop 0
	global_load_lds_dwordx4 v149, s[30:31]
	s_waitcnt vmcnt(8)
	s_waitcnt lgkmcnt(0)
	s_barrier
	s_setprio 1
	s_waitcnt lgkmcnt(0)
	v_mfma_f32_16x16x32_bf16 v[126:129], v[130:133], v[178:181], v[126:129]
	v_mfma_f32_16x16x32_bf16 v[122:125], v[154:157], v[178:181], v[122:125]
	v_mfma_f32_16x16x32_bf16 v[118:121], v[130:133], v[186:189], v[118:121]
	v_mfma_f32_16x16x32_bf16 v[110:113], v[154:157], v[186:189], v[110:113]
	v_mfma_f32_16x16x32_bf16 v[102:105], v[130:133], v[194:197], v[102:105]
	v_mfma_f32_16x16x32_bf16 v[94:97], v[154:157], v[194:197], v[94:97]
	v_mfma_f32_16x16x32_bf16 v[86:89], v[130:133], v[202:205], v[86:89]
	v_mfma_f32_16x16x32_bf16 v[78:81], v[154:157], v[202:205], v[78:81]
	v_mfma_f32_16x16x32_bf16 v[126:129], v[134:137], v[182:185], v[126:129]
	v_mfma_f32_16x16x32_bf16 v[122:125], v[158:161], v[182:185], v[122:125]
	v_mfma_f32_16x16x32_bf16 v[118:121], v[134:137], v[190:193], v[118:121]
	v_mfma_f32_16x16x32_bf16 v[110:113], v[158:161], v[190:193], v[110:113]
	v_mfma_f32_16x16x32_bf16 v[102:105], v[134:137], v[198:201], v[102:105]
	v_mfma_f32_16x16x32_bf16 v[94:97], v[158:161], v[198:201], v[94:97]
	v_mfma_f32_16x16x32_bf16 v[86:89], v[134:137], v[206:209], v[86:89]
	v_mfma_f32_16x16x32_bf16 v[78:81], v[158:161], v[206:209], v[78:81]
	s_setprio 0
	s_setprio 1
	v_mfma_f32_16x16x32_bf16 v[114:117], v[162:165], v[178:181], v[114:117]
	v_mfma_f32_16x16x32_bf16 v[106:109], v[170:173], v[178:181], v[106:109]
	v_mfma_f32_16x16x32_bf16 v[98:101], v[162:165], v[186:189], v[98:101]
	v_mfma_f32_16x16x32_bf16 v[90:93], v[170:173], v[186:189], v[90:93]
	v_mfma_f32_16x16x32_bf16 v[82:85], v[162:165], v[194:197], v[82:85]
	v_mfma_f32_16x16x32_bf16 v[74:77], v[170:173], v[194:197], v[74:77]
	v_mfma_f32_16x16x32_bf16 v[70:73], v[162:165], v[202:205], v[70:73]
	v_mfma_f32_16x16x32_bf16 v[66:69], v[170:173], v[202:205], v[66:69]
	v_mfma_f32_16x16x32_bf16 v[114:117], v[166:169], v[182:185], v[114:117]
	v_mfma_f32_16x16x32_bf16 v[106:109], v[174:177], v[182:185], v[106:109]
	v_mfma_f32_16x16x32_bf16 v[98:101], v[166:169], v[190:193], v[98:101]
	v_mfma_f32_16x16x32_bf16 v[90:93], v[174:177], v[190:193], v[90:93]
	v_mfma_f32_16x16x32_bf16 v[82:85], v[166:169], v[198:201], v[82:85]
	v_mfma_f32_16x16x32_bf16 v[74:77], v[174:177], v[198:201], v[74:77]
	v_mfma_f32_16x16x32_bf16 v[70:73], v[166:169], v[206:209], v[70:73]
	v_mfma_f32_16x16x32_bf16 v[66:69], v[174:177], v[206:209], v[66:69]
	s_setprio 0
	s_barrier
	v_mov_b32_e32 v0, v145
	ds_read_b128 v[178:181], v152 offset:49152
	ds_read_b128 v[182:185], v152 offset:50176
	ds_read_b128 v[186:189], v152 offset:51200
	ds_read_b128 v[190:193], v152 offset:52224
	ds_read_b128 v[194:197], v152 offset:53248
	ds_read_b128 v[198:201], v152 offset:54272
	ds_read_b128 v[202:205], v152 offset:55296
	ds_read_b128 v[206:209], v152 offset:56320
	s_mov_b32 m0, s53
	v_lshl_add_u64 v[138:139], s[26:27], 0, v[0:1]
	v_lshl_add_u64 v[138:139], v[138:139], 0, s[90:91]
	v_mov_b32_e32 v0, v150
	global_load_lds_dwordx4 v[138:139], off
	s_mov_b32 m0, s54
	v_lshl_add_u64 v[138:139], s[26:27], 0, v[0:1]
	v_lshl_add_u64 v[138:139], v[138:139], 0, s[90:91]
	global_load_lds_dwordx4 v[138:139], off
	s_mov_b32 m0, s55
	s_nop 0
	global_load_lds_dwordx4 v145, s[28:29]
	s_mov_b32 m0, s56
	s_nop 0
	global_load_lds_dwordx4 v150, s[28:29]
	v_mov_b32_e32 v0, v141
	s_mov_b32 m0, s41
	v_lshl_add_u64 v[138:139], s[24:25], 0, v[0:1]
	v_lshl_add_u64 v[138:139], v[138:139], 0, s[90:91]
	v_mov_b32_e32 v0, v149
	global_load_lds_dwordx4 v[138:139], off
	s_mov_b32 m0, s42
	v_lshl_add_u64 v[138:139], s[24:25], 0, v[0:1]
	v_lshl_add_u64 v[138:139], v[138:139], 0, s[90:91]
	global_load_lds_dwordx4 v[138:139], off
	s_waitcnt vmcnt(8)
	s_waitcnt lgkmcnt(0)
	s_barrier
	s_setprio 1
	s_waitcnt lgkmcnt(0)
	v_mfma_f32_16x16x32_bf16 v[62:65], v[130:133], v[178:181], v[62:65]
	v_mfma_f32_16x16x32_bf16 v[58:61], v[154:157], v[178:181], v[58:61]
	v_mfma_f32_16x16x32_bf16 v[54:57], v[130:133], v[186:189], v[54:57]
	v_mfma_f32_16x16x32_bf16 v[46:49], v[154:157], v[186:189], v[46:49]
	v_mfma_f32_16x16x32_bf16 v[38:41], v[130:133], v[194:197], v[38:41]
	v_mfma_f32_16x16x32_bf16 v[30:33], v[154:157], v[194:197], v[30:33]
	v_mfma_f32_16x16x32_bf16 v[22:25], v[130:133], v[202:205], v[22:25]
	v_mfma_f32_16x16x32_bf16 v[14:17], v[154:157], v[202:205], v[14:17]
	v_mfma_f32_16x16x32_bf16 v[62:65], v[134:137], v[182:185], v[62:65]
	v_mfma_f32_16x16x32_bf16 v[58:61], v[158:161], v[182:185], v[58:61]
	v_mfma_f32_16x16x32_bf16 v[54:57], v[134:137], v[190:193], v[54:57]
	v_mfma_f32_16x16x32_bf16 v[46:49], v[158:161], v[190:193], v[46:49]
	v_mfma_f32_16x16x32_bf16 v[38:41], v[134:137], v[198:201], v[38:41]
	v_mfma_f32_16x16x32_bf16 v[30:33], v[158:161], v[198:201], v[30:33]
	v_mfma_f32_16x16x32_bf16 v[22:25], v[134:137], v[206:209], v[22:25]
	v_mfma_f32_16x16x32_bf16 v[14:17], v[158:161], v[206:209], v[14:17]
	s_setprio 0
	s_setprio 1
	v_mfma_f32_16x16x32_bf16 v[50:53], v[162:165], v[178:181], v[50:53]
	v_mfma_f32_16x16x32_bf16 v[42:45], v[170:173], v[178:181], v[42:45]
	v_mfma_f32_16x16x32_bf16 v[34:37], v[162:165], v[186:189], v[34:37]
	v_mfma_f32_16x16x32_bf16 v[26:29], v[170:173], v[186:189], v[26:29]
	v_mfma_f32_16x16x32_bf16 v[18:21], v[162:165], v[194:197], v[18:21]
	v_mfma_f32_16x16x32_bf16 v[10:13], v[170:173], v[194:197], v[10:13]
	v_mfma_f32_16x16x32_bf16 v[6:9], v[162:165], v[202:205], v[6:9]
	v_mfma_f32_16x16x32_bf16 v[2:5], v[170:173], v[202:205], v[2:5]
	v_mfma_f32_16x16x32_bf16 v[50:53], v[166:169], v[182:185], v[50:53]
	v_mfma_f32_16x16x32_bf16 v[42:45], v[174:177], v[182:185], v[42:45]
	v_mfma_f32_16x16x32_bf16 v[34:37], v[166:169], v[190:193], v[34:37]
	v_mfma_f32_16x16x32_bf16 v[26:29], v[174:177], v[190:193], v[26:29]
	v_mfma_f32_16x16x32_bf16 v[18:21], v[166:169], v[198:201], v[18:21]
	v_mfma_f32_16x16x32_bf16 v[10:13], v[174:177], v[198:201], v[10:13]
	v_mfma_f32_16x16x32_bf16 v[6:9], v[166:169], v[206:209], v[6:9]
	v_mfma_f32_16x16x32_bf16 v[2:5], v[174:177], v[206:209], v[2:5]
	s_setprio 0
	s_barrier
	s_mov_b64 s[26:27], -1
	s_andn2_b64 vcc, exec, s[22:23]
	s_mov_b64 s[22:23], 0
	s_mov_b64 s[28:29], 0x100
	s_cbranch_vccz .LBB0_918
	v_mbcnt_lo_u32_b32 v0, -1, 0
	v_mbcnt_hi_u32_b32 v0, -1, v0
	v_mov_b64_e32 v[210:211], s[8:9]
	v_and_or_b32 v218, v0, 15, s57
	s_movk_i32 s23, 0x50
	v_mad_i64_i32 v[130:131], s[14:15], v218, s23, v[210:211]
	v_or_b32_e32 v146, 16, v218
	global_load_dwordx4 v[154:157], v[130:131], off offset:48
	global_load_dwordx4 v[158:161], v[130:131], off offset:64
	v_mad_i64_i32 v[130:131], s[14:15], v146, s23, v[210:211]
	v_or_b32_e32 v142, 32, v218
	global_load_dwordx4 v[162:165], v[130:131], off offset:48
	global_load_dwordx4 v[166:169], v[130:131], off offset:64
	v_mad_i64_i32 v[130:131], s[14:15], v142, s23, v[210:211]
	global_load_dwordx4 v[170:173], v[130:131], off offset:48
	global_load_dwordx4 v[174:177], v[130:131], off offset:64
	v_or_b32_e32 v138, 48, v218
	v_mad_i64_i32 v[130:131], s[14:15], v138, s23, v[210:211]
	global_load_dwordx4 v[178:181], v[130:131], off offset:48
	global_load_dwordx4 v[182:185], v[130:131], off offset:64
	v_add_u32_e32 v136, 0x80, v218
	v_mad_i64_i32 v[130:131], s[14:15], v136, s23, v[210:211]
	global_load_dwordx4 v[186:189], v[130:131], off offset:48
	global_load_dwordx4 v[190:193], v[130:131], off offset:64
	v_add_u32_e32 v134, 0x90, v218
	v_mad_i64_i32 v[130:131], s[20:21], v134, s23, v[210:211]
	global_load_dwordx4 v[194:197], v[130:131], off offset:48
	global_load_dwordx4 v[198:201], v[130:131], off offset:64
	v_add_u32_e32 v132, 0xa0, v218
	v_mad_i64_i32 v[206:207], s[20:21], v132, s23, v[210:211]
	global_load_dwordx4 v[202:205], v[206:207], off offset:48
	s_nop 0
	global_load_dwordx4 v[206:209], v[206:207], off offset:64
	v_add_u32_e32 v130, 0xb0, v218
	v_mad_i64_i32 v[214:215], s[20:21], v130, s23, v[210:211]
	global_load_dwordx4 v[210:213], v[214:215], off offset:48
	s_nop 0
	global_load_dwordx4 v[214:217], v[214:215], off offset:64
	v_readlane_b32 vcc_lo, v254, 19
	v_readlane_b32 vcc_hi, v254, 20
	s_and_b64 vcc, exec, vcc
	s_cbranch_vccz .LBB0_921
	s_barrier
.LBB0_921:
	s_cmp_lt_u32 s58, 2
	s_mov_b32 s14, 0x1d000000
	s_cselect_b32 s14, s14, 0x1e000000
	s_add_u32 s14, s0, s14
	s_addc_u32 s15, s1, 0
	s_lshl_b32 s22, s58, 8
	s_and_b32 s20, s22, 0x100
	v_lshrrev_b32_e32 v0, 1, v0
	v_ashrrev_i32_e32 v219, 31, v218
	v_and_or_b32 v0, v0, 24, s20
	v_or_b32_e32 v0, s72, v0
	v_lshlrev_b32_e32 v0, 1, v0
	v_ashrrev_i32_e32 v147, 31, v146
	v_ashrrev_i32_e32 v143, 31, v142
	v_ashrrev_i32_e32 v139, 31, v138
	v_ashrrev_i32_e32 v137, 31, v136
	v_ashrrev_i32_e32 v135, 31, v134
	v_ashrrev_i32_e32 v133, 31, v132
	v_ashrrev_i32_e32 v131, 31, v130
	s_andn2_b64 vcc, exec, s[12:13]
	s_mov_b64 s[12:13], -1
	s_waitcnt vmcnt(0)
	v_mov_b32_e32 v220, v154
	v_mov_b32_e32 v221, v158
	v_mov_b32_e32 v158, v155
	v_mov_b32_e32 v154, v156
	v_mov_b32_e32 v155, v160
	v_mov_b32_e32 v160, v157
	v_pk_add_f32 v[156:157], v[220:221], v[158:159]
	v_pk_add_f32 v[154:155], v[154:155], v[160:161]
	v_mov_b32_e32 v158, v162
	v_mov_b32_e32 v159, v166
	v_mov_b32_e32 v166, v163
	v_mov_b32_e32 v160, v164
	v_mov_b32_e32 v161, v168
	v_mov_b32_e32 v168, v165
	v_mov_b32_e32 v162, v170
	v_mov_b32_e32 v163, v174
	v_mov_b32_e32 v174, v171
	v_mov_b32_e32 v164, v172
	v_mov_b32_e32 v165, v176
	v_mov_b32_e32 v176, v173
	v_pk_add_f32 v[154:155], v[156:157], v[154:155]
	v_pk_add_f32 v[156:157], v[158:159], v[166:167]
	v_pk_add_f32 v[158:159], v[160:161], v[168:169]
	v_pk_add_f32 v[160:161], v[162:163], v[174:175]
	v_pk_add_f32 v[162:163], v[164:165], v[176:177]
	v_add_f32_e32 v140, v154, v155
	v_pk_add_f32 v[154:155], v[156:157], v[158:159]
	v_pk_add_f32 v[156:157], v[160:161], v[162:163]
	v_mov_b32_e32 v160, v178
	v_mov_b32_e32 v161, v182
	v_mov_b32_e32 v182, v179
	v_mov_b32_e32 v162, v180
	v_mov_b32_e32 v163, v184
	v_mov_b32_e32 v184, v181
	v_fmamk_f32 v140, v140, 0x3b800000, v232
	v_add_f32_e32 v144, v154, v155
	v_pk_add_f32 v[160:161], v[160:161], v[182:183]
	v_pk_add_f32 v[162:163], v[162:163], v[184:185]
	v_rsq_f32_e32 v154, v140
	v_fmamk_f32 v140, v144, 0x3b800000, v232
	v_pk_add_f32 v[160:161], v[160:161], v[162:163]
	v_mov_b32_e32 v162, v186
	v_mov_b32_e32 v163, v190
	v_mov_b32_e32 v190, v187
	v_mov_b32_e32 v164, v188
	v_mov_b32_e32 v165, v192
	v_mov_b32_e32 v192, v189
	v_add_f32_e32 v148, v156, v157
	v_rsq_f32_e32 v156, v140
	v_add_f32_e32 v140, v160, v161
	v_pk_add_f32 v[162:163], v[162:163], v[190:191]
	v_pk_add_f32 v[164:165], v[164:165], v[192:193]
	v_fmamk_f32 v140, v140, 0x3b800000, v232
	v_pk_add_f32 v[162:163], v[162:163], v[164:165]
	v_mov_b32_e32 v164, v194
	v_mov_b32_e32 v165, v198
	v_mov_b32_e32 v198, v195
	v_mov_b32_e32 v166, v196
	v_mov_b32_e32 v167, v200
	v_mov_b32_e32 v200, v197
	v_rsq_f32_e32 v160, v140
	v_add_f32_e32 v140, v162, v163
	v_pk_add_f32 v[164:165], v[164:165], v[198:199]
	v_pk_add_f32 v[166:167], v[166:167], v[200:201]
	v_fmamk_f32 v140, v140, 0x3b800000, v232
	v_pk_add_f32 v[164:165], v[164:165], v[166:167]
	v_rsq_f32_e32 v162, v140
	v_add_f32_e32 v140, v164, v165
	v_mov_b32_e32 v164, v202
	v_mov_b32_e32 v165, v206
	v_mov_b32_e32 v206, v203
	v_mov_b32_e32 v166, v204
	v_mov_b32_e32 v167, v208
	v_mov_b32_e32 v208, v205
	v_pk_add_f32 v[164:165], v[164:165], v[206:207]
	v_pk_add_f32 v[166:167], v[166:167], v[208:209]
	v_fmamk_f32 v140, v140, 0x3b800000, v232
	v_pk_add_f32 v[164:165], v[164:165], v[166:167]
	v_fmamk_f32 v144, v148, 0x3b800000, v232
	v_rsq_f32_e32 v148, v140
	v_add_f32_e32 v140, v164, v165
	v_mov_b32_e32 v164, v210
	v_mov_b32_e32 v165, v214
	v_mov_b32_e32 v214, v211
	v_mov_b32_e32 v166, v212
	v_mov_b32_e32 v167, v216
	v_mov_b32_e32 v216, v213
	v_pk_add_f32 v[164:165], v[164:165], v[214:215]
	v_pk_add_f32 v[166:167], v[166:167], v[216:217]
	v_fmamk_f32 v140, v140, 0x3b800000, v232
	v_pk_add_f32 v[164:165], v[164:165], v[166:167]
	v_rsq_f32_e32 v158, v144
	v_rsq_f32_e32 v144, v140
	v_add_f32_e32 v140, v164, v165
	v_lshlrev_b64 v[164:165], 10, v[218:219]
	v_lshl_add_u64 v[164:165], s[14:15], 0, v[164:165]
	v_pk_mul_f32 v[128:129], v[128:129], v[154:155] op_sel_hi:[1,0]
	v_pk_mul_f32 v[126:127], v[126:127], v[154:155] op_sel_hi:[1,0]
	v_pk_mul_f32 v[166:167], v[124:125], v[154:155] op_sel_hi:[1,0]
	v_pk_mul_f32 v[124:125], v[122:123], v[154:155] op_sel_hi:[1,0]
	v_lshl_add_u64 v[164:165], v[164:165], 0, v[0:1]
	v_cvt_pk_bf16_f32 v122, v126, v127
	v_cvt_pk_bf16_f32 v123, v128, v129
	v_cvt_pk_bf16_f32 v124, v124, v125
	v_cvt_pk_bf16_f32 v125, v166, v167
	global_store_dwordx4 v[164:165], v[122:125], off
	v_pk_mul_f32 v[116:117], v[116:117], v[154:155] op_sel_hi:[1,0]
	v_pk_mul_f32 v[114:115], v[114:115], v[154:155] op_sel_hi:[1,0]
	v_pk_mul_f32 v[122:123], v[108:109], v[154:155] op_sel_hi:[1,0]
	v_pk_mul_f32 v[108:109], v[106:107], v[154:155] op_sel_hi:[1,0]
	v_cvt_pk_bf16_f32 v106, v114, v115
	v_cvt_pk_bf16_f32 v107, v116, v117
	v_cvt_pk_bf16_f32 v108, v108, v109
	v_cvt_pk_bf16_f32 v109, v122, v123
	global_store_dwordx4 v[164:165], v[106:109], off offset:256
	v_pk_mul_f32 v[112:113], v[112:113], v[156:157] op_sel_hi:[1,0]
	v_pk_mul_f32 v[110:111], v[110:111], v[156:157] op_sel_hi:[1,0]
	v_lshlrev_b64 v[106:107], 10, v[146:147]
	v_lshl_add_u64 v[106:107], s[14:15], 0, v[106:107]
	v_lshl_add_u64 v[114:115], v[106:107], 0, v[0:1]
	v_pk_mul_f32 v[108:109], v[120:121], v[156:157] op_sel_hi:[1,0]
	v_pk_mul_f32 v[106:107], v[118:119], v[156:157] op_sel_hi:[1,0]
	v_pk_mul_f32 v[100:101], v[100:101], v[156:157] op_sel_hi:[1,0]
	v_cvt_pk_bf16_f32 v106, v106, v107
	v_cvt_pk_bf16_f32 v107, v108, v109
	v_cvt_pk_bf16_f32 v108, v110, v111
	v_cvt_pk_bf16_f32 v109, v112, v113
	global_store_dwordx4 v[114:115], v[106:109], off
	v_pk_mul_f32 v[98:99], v[98:99], v[156:157] op_sel_hi:[1,0]
	v_pk_mul_f32 v[96:97], v[96:97], v[158:159] op_sel_hi:[1,0]
	v_pk_mul_f32 v[106:107], v[92:93], v[156:157] op_sel_hi:[1,0]
	v_pk_mul_f32 v[92:93], v[90:91], v[156:157] op_sel_hi:[1,0]
	v_cvt_pk_bf16_f32 v90, v98, v99
	v_cvt_pk_bf16_f32 v91, v100, v101
	v_cvt_pk_bf16_f32 v92, v92, v93
	v_cvt_pk_bf16_f32 v93, v106, v107
	global_store_dwordx4 v[114:115], v[90:93], off offset:256
	v_pk_mul_f32 v[94:95], v[94:95], v[158:159] op_sel_hi:[1,0]
	v_pk_mul_f32 v[84:85], v[84:85], v[158:159] op_sel_hi:[1,0]
	v_lshlrev_b64 v[90:91], 10, v[142:143]
	v_lshl_add_u64 v[90:91], s[14:15], 0, v[90:91]
	v_lshl_add_u64 v[98:99], v[90:91], 0, v[0:1]
	v_pk_mul_f32 v[92:93], v[104:105], v[158:159] op_sel_hi:[1,0]
	v_pk_mul_f32 v[90:91], v[102:103], v[158:159] op_sel_hi:[1,0]
	v_pk_mul_f32 v[82:83], v[82:83], v[158:159] op_sel_hi:[1,0]
	v_cvt_pk_bf16_f32 v90, v90, v91
	v_cvt_pk_bf16_f32 v91, v92, v93
	v_cvt_pk_bf16_f32 v92, v94, v95
	v_cvt_pk_bf16_f32 v93, v96, v97
	global_store_dwordx4 v[98:99], v[90:93], off
	v_pk_mul_f32 v[80:81], v[80:81], v[160:161] op_sel_hi:[1,0]
	v_pk_mul_f32 v[78:79], v[78:79], v[160:161] op_sel_hi:[1,0]
	v_pk_mul_f32 v[90:91], v[76:77], v[158:159] op_sel_hi:[1,0]
	v_pk_mul_f32 v[76:77], v[74:75], v[158:159] op_sel_hi:[1,0]
	v_cvt_pk_bf16_f32 v74, v82, v83
	v_cvt_pk_bf16_f32 v75, v84, v85
	v_cvt_pk_bf16_f32 v76, v76, v77
	v_cvt_pk_bf16_f32 v77, v90, v91
	global_store_dwordx4 v[98:99], v[74:77], off offset:256
	v_pk_mul_f32 v[72:73], v[72:73], v[160:161] op_sel_hi:[1,0]
	v_pk_mul_f32 v[70:71], v[70:71], v[160:161] op_sel_hi:[1,0]
	v_lshlrev_b64 v[74:75], 10, v[138:139]
	v_lshl_add_u64 v[74:75], s[14:15], 0, v[74:75]
	v_lshl_add_u64 v[82:83], v[74:75], 0, v[0:1]
	v_pk_mul_f32 v[76:77], v[88:89], v[160:161] op_sel_hi:[1,0]
	v_pk_mul_f32 v[74:75], v[86:87], v[160:161] op_sel_hi:[1,0]
	v_pk_mul_f32 v[64:65], v[64:65], v[162:163] op_sel_hi:[1,0]
	v_cvt_pk_bf16_f32 v74, v74, v75
	v_cvt_pk_bf16_f32 v75, v76, v77
	v_cvt_pk_bf16_f32 v76, v78, v79
	v_cvt_pk_bf16_f32 v77, v80, v81
	global_store_dwordx4 v[82:83], v[74:77], off
	v_pk_mul_f32 v[62:63], v[62:63], v[162:163] op_sel_hi:[1,0]
	v_pk_mul_f32 v[52:53], v[52:53], v[162:163] op_sel_hi:[1,0]
	v_pk_mul_f32 v[74:75], v[68:69], v[160:161] op_sel_hi:[1,0]
	v_pk_mul_f32 v[68:69], v[66:67], v[160:161] op_sel_hi:[1,0]
	v_cvt_pk_bf16_f32 v66, v70, v71
	v_cvt_pk_bf16_f32 v67, v72, v73
	v_cvt_pk_bf16_f32 v68, v68, v69
	v_cvt_pk_bf16_f32 v69, v74, v75
	global_store_dwordx4 v[82:83], v[66:69], off offset:256
	v_pk_mul_f32 v[50:51], v[50:51], v[162:163] op_sel_hi:[1,0]
	v_pk_mul_f32 v[48:49], v[48:49], v[148:149] op_sel_hi:[1,0]
	v_lshlrev_b64 v[66:67], 10, v[136:137]
	v_lshl_add_u64 v[66:67], s[14:15], 0, v[66:67]
	v_pk_mul_f32 v[68:69], v[60:61], v[162:163] op_sel_hi:[1,0]
	v_pk_mul_f32 v[60:61], v[58:59], v[162:163] op_sel_hi:[1,0]
	v_lshl_add_u64 v[66:67], v[66:67], 0, v[0:1]
	v_cvt_pk_bf16_f32 v58, v62, v63
	v_cvt_pk_bf16_f32 v59, v64, v65
	v_cvt_pk_bf16_f32 v60, v60, v61
	v_cvt_pk_bf16_f32 v61, v68, v69
	global_store_dwordx4 v[66:67], v[58:61], off
	v_pk_mul_f32 v[46:47], v[46:47], v[148:149] op_sel_hi:[1,0]
	v_pk_mul_f32 v[36:37], v[36:37], v[148:149] op_sel_hi:[1,0]
	v_pk_mul_f32 v[58:59], v[44:45], v[162:163] op_sel_hi:[1,0]
	v_pk_mul_f32 v[44:45], v[42:43], v[162:163] op_sel_hi:[1,0]
	v_cvt_pk_bf16_f32 v42, v50, v51
	v_cvt_pk_bf16_f32 v43, v52, v53
	v_cvt_pk_bf16_f32 v44, v44, v45
	v_cvt_pk_bf16_f32 v45, v58, v59
	global_store_dwordx4 v[66:67], v[42:45], off offset:256
	v_pk_mul_f32 v[34:35], v[34:35], v[148:149] op_sel_hi:[1,0]
	v_pk_mul_f32 v[32:33], v[32:33], v[144:145] op_sel_hi:[1,0]
	v_lshlrev_b64 v[42:43], 10, v[134:135]
	v_lshl_add_u64 v[42:43], s[14:15], 0, v[42:43]
	v_lshl_add_u64 v[50:51], v[42:43], 0, v[0:1]
	v_pk_mul_f32 v[44:45], v[56:57], v[148:149] op_sel_hi:[1,0]
	v_pk_mul_f32 v[42:43], v[54:55], v[148:149] op_sel_hi:[1,0]
	v_pk_mul_f32 v[30:31], v[30:31], v[144:145] op_sel_hi:[1,0]
	v_cvt_pk_bf16_f32 v42, v42, v43
	v_cvt_pk_bf16_f32 v43, v44, v45
	v_cvt_pk_bf16_f32 v44, v46, v47
	v_cvt_pk_bf16_f32 v45, v48, v49
	global_store_dwordx4 v[50:51], v[42:45], off
	v_fmamk_f32 v140, v140, 0x3b800000, v232
	v_rsq_f32_e32 v140, v140
	v_pk_mul_f32 v[42:43], v[28:29], v[148:149] op_sel_hi:[1,0]
	v_pk_mul_f32 v[28:29], v[26:27], v[148:149] op_sel_hi:[1,0]
	v_cvt_pk_bf16_f32 v26, v34, v35
	v_cvt_pk_bf16_f32 v27, v36, v37
	v_cvt_pk_bf16_f32 v28, v28, v29
	v_cvt_pk_bf16_f32 v29, v42, v43
	global_store_dwordx4 v[50:51], v[26:29], off offset:256
	v_pk_mul_f32 v[20:21], v[20:21], v[144:145] op_sel_hi:[1,0]
	v_pk_mul_f32 v[18:19], v[18:19], v[144:145] op_sel_hi:[1,0]
	v_lshlrev_b64 v[26:27], 10, v[132:133]
	v_lshl_add_u64 v[26:27], s[14:15], 0, v[26:27]
	v_lshl_add_u64 v[34:35], v[26:27], 0, v[0:1]
	v_pk_mul_f32 v[28:29], v[40:41], v[144:145] op_sel_hi:[1,0]
	v_pk_mul_f32 v[26:27], v[38:39], v[144:145] op_sel_hi:[1,0]
	v_pk_mul_f32 v[16:17], v[16:17], v[140:141] op_sel_hi:[1,0]
	v_cvt_pk_bf16_f32 v26, v26, v27
	v_cvt_pk_bf16_f32 v27, v28, v29
	v_cvt_pk_bf16_f32 v28, v30, v31
	v_cvt_pk_bf16_f32 v29, v32, v33
	global_store_dwordx4 v[34:35], v[26:29], off
	v_pk_mul_f32 v[14:15], v[14:15], v[140:141] op_sel_hi:[1,0]
	v_pk_mul_f32 v[8:9], v[8:9], v[140:141] op_sel_hi:[1,0]
	v_pk_mul_f32 v[26:27], v[12:13], v[144:145] op_sel_hi:[1,0]
	v_pk_mul_f32 v[12:13], v[10:11], v[144:145] op_sel_hi:[1,0]
	v_cvt_pk_bf16_f32 v10, v18, v19
	v_cvt_pk_bf16_f32 v11, v20, v21
	v_cvt_pk_bf16_f32 v12, v12, v13
	v_cvt_pk_bf16_f32 v13, v26, v27
	global_store_dwordx4 v[34:35], v[10:13], off offset:256
	v_pk_mul_f32 v[6:7], v[6:7], v[140:141] op_sel_hi:[1,0]
	s_nop 0
	v_lshlrev_b64 v[10:11], 10, v[130:131]
	v_lshl_add_u64 v[10:11], s[14:15], 0, v[10:11]
	v_lshl_add_u64 v[18:19], v[10:11], 0, v[0:1]
	v_pk_mul_f32 v[12:13], v[24:25], v[140:141] op_sel_hi:[1,0]
	v_pk_mul_f32 v[10:11], v[22:23], v[140:141] op_sel_hi:[1,0]
	s_nop 0
	v_cvt_pk_bf16_f32 v10, v10, v11
	v_cvt_pk_bf16_f32 v11, v12, v13
	v_cvt_pk_bf16_f32 v12, v14, v15
	v_cvt_pk_bf16_f32 v13, v16, v17
	global_store_dwordx4 v[18:19], v[10:13], off
	s_nop 1
	v_pk_mul_f32 v[10:11], v[4:5], v[140:141] op_sel_hi:[1,0]
	v_pk_mul_f32 v[4:5], v[2:3], v[140:141] op_sel_hi:[1,0]
	v_cvt_pk_bf16_f32 v2, v6, v7
	v_cvt_pk_bf16_f32 v3, v8, v9
	v_cvt_pk_bf16_f32 v4, v4, v5
	v_cvt_pk_bf16_f32 v5, v10, v11
	global_store_dwordx4 v[18:19], v[2:5], off offset:256
	s_cbranch_vccnz .LBB0_916
	s_and_b64 vcc, exec, s[6:7]
	s_cbranch_vccnz .LBB0_915
	s_barrier
	s_branch .LBB0_915

.LBB0_1658:
	s_ashr_i32 s22, s26, 3
	s_add_i32 s22, s28, s22
	s_ashr_i32 s23, s22, 31
	s_lshr_b32 s23, s23, 27
	s_add_i32 s26, s22, s23
	s_ashr_i32 s23, s26, 5
	s_lshl_b32 s27, s23, 3
	s_sub_i32 s23, s13, s27
	s_min_i32 s28, s23, 8
	s_abs_i32 s29, s28
	v_cvt_f32_u32_e32 v0, s29
	s_sub_i32 s58, 0, s29
	s_andn2_b32 s26, s26, 31
	s_sub_i32 s22, s22, s26
	v_rcp_iflag_f32_e32 v0, v0
	s_abs_i32 s26, s22
	s_xor_b32 s56, s22, s28
	s_ashr_i32 s56, s56, 31
	v_mul_f32_e32 v0, 0x4f7ffffe, v0
	v_cvt_u32_f32_e32 v0, v0
	s_mov_b32 s23, 0
	v_readfirstlane_b32 s59, v0
	s_mul_i32 s58, s58, s59
	s_mul_hi_u32 s58, s59, s58
	s_add_i32 s59, s59, s58
	s_mul_hi_u32 s58, s26, s59
	s_mul_i32 s59, s58, s29
	s_sub_i32 s26, s26, s59
	s_add_i32 s60, s58, 1
	s_sub_i32 s59, s26, s29
	s_cmp_ge_u32 s26, s29
	s_cselect_b32 s58, s60, s58
	s_cselect_b32 s26, s59, s26
	s_add_i32 s59, s58, 1
	s_cmp_ge_u32 s26, s29
	s_cselect_b32 s26, s59, s58
	s_xor_b32 s26, s26, s56
	s_sub_i32 s56, s26, s56
	s_mul_i32 s26, s56, s28
	s_sub_i32 s22, s22, s26
	s_andn2_b64 vcc, exec, s[18:19]
	s_add_i32 s22, s27, s22
	s_cbranch_vccnz .LBB0_1660
	s_lshl_b32 s26, s22, 2
	s_add_i32 s26, s26, 0x21000
	v_mov_b32_e32 v0, s26
	ds_read_b32 v0, v0
	s_waitcnt lgkmcnt(0)
	v_readfirstlane_b32 s23, v0
